# router logits GEMM: 8 straight-line K steps with all eight fragment loads of a step in flight (was 3-4 exposed load round trips per step), on top of v77
# baseline (speedup 1.0000x reference)
.LBB0_1028:
	v_lshl_add_u64 v[100:101], v[84:85], 0, s[42:43]
	v_lshl_add_u64 v[98:99], v[74:75], 0, s[42:43]
	s_mov_b32 s27, 0
	s_mov_b32 s26, s44
	v_lshl_add_u64 v[86:87], v[100:101], 0, s[26:27]
	v_lshl_add_u64 v[92:93], v[98:99], 0, s[26:27]
	s_mov_b32 s26, s45
	v_lshl_add_u64 v[68:69], v[100:101], 0, s[26:27]
	v_lshl_add_u64 v[90:91], v[98:99], 0, s[26:27]
	s_mov_b32 s26, s46
	v_lshl_add_u64 v[70:71], v[100:101], 0, s[26:27]
	v_lshl_add_u64 v[88:89], v[98:99], 0, s[26:27]
	global_load_dwordx4 v[222:225], v[98:99], off
	global_load_dwordx4 v[226:229], v[92:93], off
	global_load_dwordx4 v[230:233], v[90:91], off
	global_load_dwordx4 v[234:237], v[88:89], off
	global_load_dwordx4 v[94:97], v[100:101], off
	global_load_dwordx4 v[238:241], v[86:87], off
	global_load_dwordx4 v[242:245], v[68:69], off
	global_load_dwordx4 v[246:249], v[70:71], off
	s_waitcnt vmcnt(3)
	v_mfma_f32_16x16x32_bf16 v[22:25], v[94:97], v[222:225], v[22:25]
	v_mfma_f32_16x16x32_bf16 v[62:65], v[94:97], v[226:229], v[62:65]
	v_mfma_f32_16x16x32_bf16 v[58:61], v[94:97], v[230:233], v[58:61]
	v_mfma_f32_16x16x32_bf16 v[54:57], v[94:97], v[234:237], v[54:57]
	global_load_dwordx4 v[94:97], v[100:101], off offset:64
	s_waitcnt vmcnt(3)
	v_mfma_f32_16x16x32_bf16 v[50:53], v[238:241], v[222:225], v[50:53]
	v_mfma_f32_16x16x32_bf16 v[46:49], v[238:241], v[226:229], v[46:49]
	v_mfma_f32_16x16x32_bf16 v[42:45], v[238:241], v[230:233], v[42:45]
	v_mfma_f32_16x16x32_bf16 v[38:41], v[238:241], v[234:237], v[38:41]
	global_load_dwordx4 v[238:241], v[86:87], off offset:64
	s_waitcnt vmcnt(3)
	v_mfma_f32_16x16x32_bf16 v[34:37], v[242:245], v[222:225], v[34:37]
	v_mfma_f32_16x16x32_bf16 v[18:21], v[242:245], v[226:229], v[18:21]
	v_mfma_f32_16x16x32_bf16 v[10:13], v[242:245], v[230:233], v[10:13]
	v_mfma_f32_16x16x32_bf16 v[2:5], v[242:245], v[234:237], v[2:5]
	global_load_dwordx4 v[242:245], v[68:69], off offset:64
	s_waitcnt vmcnt(3)
	v_mfma_f32_16x16x32_bf16 v[26:29], v[246:249], v[222:225], v[26:29]
	v_mfma_f32_16x16x32_bf16 v[14:17], v[246:249], v[226:229], v[14:17]
	v_mfma_f32_16x16x32_bf16 v[6:9], v[246:249], v[230:233], v[6:9]
	v_mfma_f32_16x16x32_bf16 v[30:33], v[246:249], v[234:237], v[30:33]
	global_load_dwordx4 v[246:249], v[70:71], off offset:64
	global_load_dwordx4 v[222:225], v[98:99], off offset:64
	global_load_dwordx4 v[226:229], v[92:93], off offset:64
	global_load_dwordx4 v[230:233], v[90:91], off offset:64
	global_load_dwordx4 v[234:237], v[88:89], off offset:64
	s_waitcnt vmcnt(0)
	v_mfma_f32_16x16x32_bf16 v[22:25], v[94:97], v[222:225], v[22:25]
	v_mfma_f32_16x16x32_bf16 v[62:65], v[94:97], v[226:229], v[62:65]
	v_mfma_f32_16x16x32_bf16 v[58:61], v[94:97], v[230:233], v[58:61]
	v_mfma_f32_16x16x32_bf16 v[54:57], v[94:97], v[234:237], v[54:57]
	global_load_dwordx4 v[94:97], v[100:101], off offset:128
	s_waitcnt vmcnt(3)
	v_mfma_f32_16x16x32_bf16 v[50:53], v[238:241], v[222:225], v[50:53]
	v_mfma_f32_16x16x32_bf16 v[46:49], v[238:241], v[226:229], v[46:49]
	v_mfma_f32_16x16x32_bf16 v[42:45], v[238:241], v[230:233], v[42:45]
	v_mfma_f32_16x16x32_bf16 v[38:41], v[238:241], v[234:237], v[38:41]
	global_load_dwordx4 v[238:241], v[86:87], off offset:128
	s_waitcnt vmcnt(3)
	v_mfma_f32_16x16x32_bf16 v[34:37], v[242:245], v[222:225], v[34:37]
	v_mfma_f32_16x16x32_bf16 v[18:21], v[242:245], v[226:229], v[18:21]
	v_mfma_f32_16x16x32_bf16 v[10:13], v[242:245], v[230:233], v[10:13]
	v_mfma_f32_16x16x32_bf16 v[2:5], v[242:245], v[234:237], v[2:5]
	global_load_dwordx4 v[242:245], v[68:69], off offset:128
	s_waitcnt vmcnt(3)
	v_mfma_f32_16x16x32_bf16 v[26:29], v[246:249], v[222:225], v[26:29]
	v_mfma_f32_16x16x32_bf16 v[14:17], v[246:249], v[226:229], v[14:17]
	v_mfma_f32_16x16x32_bf16 v[6:9], v[246:249], v[230:233], v[6:9]
	v_mfma_f32_16x16x32_bf16 v[30:33], v[246:249], v[234:237], v[30:33]
	global_load_dwordx4 v[246:249], v[70:71], off offset:128
	global_load_dwordx4 v[222:225], v[98:99], off offset:128
	global_load_dwordx4 v[226:229], v[92:93], off offset:128
	global_load_dwordx4 v[230:233], v[90:91], off offset:128
	global_load_dwordx4 v[234:237], v[88:89], off offset:128
	s_waitcnt vmcnt(0)
	v_mfma_f32_16x16x32_bf16 v[22:25], v[94:97], v[222:225], v[22:25]
	v_mfma_f32_16x16x32_bf16 v[62:65], v[94:97], v[226:229], v[62:65]
	v_mfma_f32_16x16x32_bf16 v[58:61], v[94:97], v[230:233], v[58:61]
	v_mfma_f32_16x16x32_bf16 v[54:57], v[94:97], v[234:237], v[54:57]
	global_load_dwordx4 v[94:97], v[100:101], off offset:192
	s_waitcnt vmcnt(3)
	v_mfma_f32_16x16x32_bf16 v[50:53], v[238:241], v[222:225], v[50:53]
	v_mfma_f32_16x16x32_bf16 v[46:49], v[238:241], v[226:229], v[46:49]
	v_mfma_f32_16x16x32_bf16 v[42:45], v[238:241], v[230:233], v[42:45]
	v_mfma_f32_16x16x32_bf16 v[38:41], v[238:241], v[234:237], v[38:41]
	global_load_dwordx4 v[238:241], v[86:87], off offset:192
	s_waitcnt vmcnt(3)
	v_mfma_f32_16x16x32_bf16 v[34:37], v[242:245], v[222:225], v[34:37]
	v_mfma_f32_16x16x32_bf16 v[18:21], v[242:245], v[226:229], v[18:21]
	v_mfma_f32_16x16x32_bf16 v[10:13], v[242:245], v[230:233], v[10:13]
	v_mfma_f32_16x16x32_bf16 v[2:5], v[242:245], v[234:237], v[2:5]
	global_load_dwordx4 v[242:245], v[68:69], off offset:192
	s_waitcnt vmcnt(3)
	v_mfma_f32_16x16x32_bf16 v[26:29], v[246:249], v[222:225], v[26:29]
	v_mfma_f32_16x16x32_bf16 v[14:17], v[246:249], v[226:229], v[14:17]
	v_mfma_f32_16x16x32_bf16 v[6:9], v[246:249], v[230:233], v[6:9]
	v_mfma_f32_16x16x32_bf16 v[30:33], v[246:249], v[234:237], v[30:33]
	global_load_dwordx4 v[246:249], v[70:71], off offset:192
	global_load_dwordx4 v[222:225], v[98:99], off offset:192
	global_load_dwordx4 v[226:229], v[92:93], off offset:192
	global_load_dwordx4 v[230:233], v[90:91], off offset:192
	global_load_dwordx4 v[234:237], v[88:89], off offset:192
	s_waitcnt vmcnt(0)
	v_mfma_f32_16x16x32_bf16 v[22:25], v[94:97], v[222:225], v[22:25]
	v_mfma_f32_16x16x32_bf16 v[62:65], v[94:97], v[226:229], v[62:65]
	v_mfma_f32_16x16x32_bf16 v[58:61], v[94:97], v[230:233], v[58:61]
	v_mfma_f32_16x16x32_bf16 v[54:57], v[94:97], v[234:237], v[54:57]
	global_load_dwordx4 v[94:97], v[100:101], off offset:256
	s_waitcnt vmcnt(3)
	v_mfma_f32_16x16x32_bf16 v[50:53], v[238:241], v[222:225], v[50:53]
	v_mfma_f32_16x16x32_bf16 v[46:49], v[238:241], v[226:229], v[46:49]
	v_mfma_f32_16x16x32_bf16 v[42:45], v[238:241], v[230:233], v[42:45]
	v_mfma_f32_16x16x32_bf16 v[38:41], v[238:241], v[234:237], v[38:41]
	global_load_dwordx4 v[238:241], v[86:87], off offset:256
	s_waitcnt vmcnt(3)
	v_mfma_f32_16x16x32_bf16 v[34:37], v[242:245], v[222:225], v[34:37]
	v_mfma_f32_16x16x32_bf16 v[18:21], v[242:245], v[226:229], v[18:21]
	v_mfma_f32_16x16x32_bf16 v[10:13], v[242:245], v[230:233], v[10:13]
	v_mfma_f32_16x16x32_bf16 v[2:5], v[242:245], v[234:237], v[2:5]
	global_load_dwordx4 v[242:245], v[68:69], off offset:256
	s_waitcnt vmcnt(3)
	v_mfma_f32_16x16x32_bf16 v[26:29], v[246:249], v[222:225], v[26:29]
	v_mfma_f32_16x16x32_bf16 v[14:17], v[246:249], v[226:229], v[14:17]
	v_mfma_f32_16x16x32_bf16 v[6:9], v[246:249], v[230:233], v[6:9]
	v_mfma_f32_16x16x32_bf16 v[30:33], v[246:249], v[234:237], v[30:33]
	global_load_dwordx4 v[246:249], v[70:71], off offset:256
	global_load_dwordx4 v[222:225], v[98:99], off offset:256
	global_load_dwordx4 v[226:229], v[92:93], off offset:256
	global_load_dwordx4 v[230:233], v[90:91], off offset:256
	global_load_dwordx4 v[234:237], v[88:89], off offset:256
	s_waitcnt vmcnt(0)
	v_mfma_f32_16x16x32_bf16 v[22:25], v[94:97], v[222:225], v[22:25]
	v_mfma_f32_16x16x32_bf16 v[62:65], v[94:97], v[226:229], v[62:65]
	v_mfma_f32_16x16x32_bf16 v[58:61], v[94:97], v[230:233], v[58:61]
	v_mfma_f32_16x16x32_bf16 v[54:57], v[94:97], v[234:237], v[54:57]
	global_load_dwordx4 v[94:97], v[100:101], off offset:320
	s_waitcnt vmcnt(3)
	v_mfma_f32_16x16x32_bf16 v[50:53], v[238:241], v[222:225], v[50:53]
	v_mfma_f32_16x16x32_bf16 v[46:49], v[238:241], v[226:229], v[46:49]
	v_mfma_f32_16x16x32_bf16 v[42:45], v[238:241], v[230:233], v[42:45]
	v_mfma_f32_16x16x32_bf16 v[38:41], v[238:241], v[234:237], v[38:41]
	global_load_dwordx4 v[238:241], v[86:87], off offset:320
	s_waitcnt vmcnt(3)
	v_mfma_f32_16x16x32_bf16 v[34:37], v[242:245], v[222:225], v[34:37]
	v_mfma_f32_16x16x32_bf16 v[18:21], v[242:245], v[226:229], v[18:21]
	v_mfma_f32_16x16x32_bf16 v[10:13], v[242:245], v[230:233], v[10:13]
	v_mfma_f32_16x16x32_bf16 v[2:5], v[242:245], v[234:237], v[2:5]
	global_load_dwordx4 v[242:245], v[68:69], off offset:320
	s_waitcnt vmcnt(3)
	v_mfma_f32_16x16x32_bf16 v[26:29], v[246:249], v[222:225], v[26:29]
	v_mfma_f32_16x16x32_bf16 v[14:17], v[246:249], v[226:229], v[14:17]
	v_mfma_f32_16x16x32_bf16 v[6:9], v[246:249], v[230:233], v[6:9]
	v_mfma_f32_16x16x32_bf16 v[30:33], v[246:249], v[234:237], v[30:33]
	global_load_dwordx4 v[246:249], v[70:71], off offset:320
	global_load_dwordx4 v[222:225], v[98:99], off offset:320
	global_load_dwordx4 v[226:229], v[92:93], off offset:320
	global_load_dwordx4 v[230:233], v[90:91], off offset:320
	global_load_dwordx4 v[234:237], v[88:89], off offset:320
	s_waitcnt vmcnt(0)
	v_mfma_f32_16x16x32_bf16 v[22:25], v[94:97], v[222:225], v[22:25]
	v_mfma_f32_16x16x32_bf16 v[62:65], v[94:97], v[226:229], v[62:65]
	v_mfma_f32_16x16x32_bf16 v[58:61], v[94:97], v[230:233], v[58:61]
	v_mfma_f32_16x16x32_bf16 v[54:57], v[94:97], v[234:237], v[54:57]
	global_load_dwordx4 v[94:97], v[100:101], off offset:384
	s_waitcnt vmcnt(3)
	v_mfma_f32_16x16x32_bf16 v[50:53], v[238:241], v[222:225], v[50:53]
	v_mfma_f32_16x16x32_bf16 v[46:49], v[238:241], v[226:229], v[46:49]
	v_mfma_f32_16x16x32_bf16 v[42:45], v[238:241], v[230:233], v[42:45]
	v_mfma_f32_16x16x32_bf16 v[38:41], v[238:241], v[234:237], v[38:41]
	global_load_dwordx4 v[238:241], v[86:87], off offset:384
	s_waitcnt vmcnt(3)
	v_mfma_f32_16x16x32_bf16 v[34:37], v[242:245], v[222:225], v[34:37]
	v_mfma_f32_16x16x32_bf16 v[18:21], v[242:245], v[226:229], v[18:21]
	v_mfma_f32_16x16x32_bf16 v[10:13], v[242:245], v[230:233], v[10:13]
	v_mfma_f32_16x16x32_bf16 v[2:5], v[242:245], v[234:237], v[2:5]
	global_load_dwordx4 v[242:245], v[68:69], off offset:384
	s_waitcnt vmcnt(3)
	v_mfma_f32_16x16x32_bf16 v[26:29], v[246:249], v[222:225], v[26:29]
	v_mfma_f32_16x16x32_bf16 v[14:17], v[246:249], v[226:229], v[14:17]
	v_mfma_f32_16x16x32_bf16 v[6:9], v[246:249], v[230:233], v[6:9]
	v_mfma_f32_16x16x32_bf16 v[30:33], v[246:249], v[234:237], v[30:33]
	global_load_dwordx4 v[246:249], v[70:71], off offset:384
	global_load_dwordx4 v[222:225], v[98:99], off offset:384
	global_load_dwordx4 v[226:229], v[92:93], off offset:384
	global_load_dwordx4 v[230:233], v[90:91], off offset:384
	global_load_dwordx4 v[234:237], v[88:89], off offset:384
	s_waitcnt vmcnt(0)
	v_mfma_f32_16x16x32_bf16 v[22:25], v[94:97], v[222:225], v[22:25]
	v_mfma_f32_16x16x32_bf16 v[62:65], v[94:97], v[226:229], v[62:65]
	v_mfma_f32_16x16x32_bf16 v[58:61], v[94:97], v[230:233], v[58:61]
	v_mfma_f32_16x16x32_bf16 v[54:57], v[94:97], v[234:237], v[54:57]
	global_load_dwordx4 v[94:97], v[100:101], off offset:448
	s_waitcnt vmcnt(3)
	v_mfma_f32_16x16x32_bf16 v[50:53], v[238:241], v[222:225], v[50:53]
	v_mfma_f32_16x16x32_bf16 v[46:49], v[238:241], v[226:229], v[46:49]
	v_mfma_f32_16x16x32_bf16 v[42:45], v[238:241], v[230:233], v[42:45]
	v_mfma_f32_16x16x32_bf16 v[38:41], v[238:241], v[234:237], v[38:41]
	global_load_dwordx4 v[238:241], v[86:87], off offset:448
	s_waitcnt vmcnt(3)
	v_mfma_f32_16x16x32_bf16 v[34:37], v[242:245], v[222:225], v[34:37]
	v_mfma_f32_16x16x32_bf16 v[18:21], v[242:245], v[226:229], v[18:21]
	v_mfma_f32_16x16x32_bf16 v[10:13], v[242:245], v[230:233], v[10:13]
	v_mfma_f32_16x16x32_bf16 v[2:5], v[242:245], v[234:237], v[2:5]
	global_load_dwordx4 v[242:245], v[68:69], off offset:448
	s_waitcnt vmcnt(3)
	v_mfma_f32_16x16x32_bf16 v[26:29], v[246:249], v[222:225], v[26:29]
	v_mfma_f32_16x16x32_bf16 v[14:17], v[246:249], v[226:229], v[14:17]
	v_mfma_f32_16x16x32_bf16 v[6:9], v[246:249], v[230:233], v[6:9]
	v_mfma_f32_16x16x32_bf16 v[30:33], v[246:249], v[234:237], v[30:33]
	global_load_dwordx4 v[246:249], v[70:71], off offset:448
	global_load_dwordx4 v[222:225], v[98:99], off offset:448
	global_load_dwordx4 v[226:229], v[92:93], off offset:448
	global_load_dwordx4 v[230:233], v[90:91], off offset:448
	global_load_dwordx4 v[234:237], v[88:89], off offset:448
	s_waitcnt vmcnt(0)
	v_mfma_f32_16x16x32_bf16 v[22:25], v[94:97], v[222:225], v[22:25]
	v_mfma_f32_16x16x32_bf16 v[62:65], v[94:97], v[226:229], v[62:65]
	v_mfma_f32_16x16x32_bf16 v[58:61], v[94:97], v[230:233], v[58:61]
	v_mfma_f32_16x16x32_bf16 v[54:57], v[94:97], v[234:237], v[54:57]
	s_waitcnt vmcnt(2)
	v_mfma_f32_16x16x32_bf16 v[50:53], v[238:241], v[222:225], v[50:53]
	v_mfma_f32_16x16x32_bf16 v[46:49], v[238:241], v[226:229], v[46:49]
	v_mfma_f32_16x16x32_bf16 v[42:45], v[238:241], v[230:233], v[42:45]
	v_mfma_f32_16x16x32_bf16 v[38:41], v[238:241], v[234:237], v[38:41]
	s_waitcnt vmcnt(1)
	v_mfma_f32_16x16x32_bf16 v[34:37], v[242:245], v[222:225], v[34:37]
	v_mfma_f32_16x16x32_bf16 v[18:21], v[242:245], v[226:229], v[18:21]
	v_mfma_f32_16x16x32_bf16 v[10:13], v[242:245], v[230:233], v[10:13]
	v_mfma_f32_16x16x32_bf16 v[2:5], v[242:245], v[234:237], v[2:5]
	s_waitcnt vmcnt(0)
	v_mfma_f32_16x16x32_bf16 v[26:29], v[246:249], v[222:225], v[26:29]
	v_mfma_f32_16x16x32_bf16 v[14:17], v[246:249], v[226:229], v[14:17]
	v_mfma_f32_16x16x32_bf16 v[6:9], v[246:249], v[230:233], v[6:9]
	v_mfma_f32_16x16x32_bf16 v[30:33], v[246:249], v[234:237], v[30:33]
	s_mov_b64 s[42:43], 0x200
	v_add_u32_e32 v83, 0x1000, v119
	ds_write2_b32 v83, v22, v62 offset1:16
	ds_write2_b32 v83, v23, v63 offset0:64 offset1:80
	ds_write2_b32 v83, v24, v64 offset0:128 offset1:144
	ds_write2_b32 v83, v25, v65 offset0:192 offset1:208
	ds_write2_b32 v83, v58, v54 offset0:32 offset1:48
	ds_write2_b32 v83, v59, v55 offset0:96 offset1:112
	ds_write2_b32 v83, v60, v56 offset0:160 offset1:176
	ds_write2_b32 v83, v61, v57 offset0:224 offset1:240
	v_add_u32_e32 v22, 0x2000, v119
	ds_write2_b32 v22, v50, v46 offset1:16
	ds_write2_b32 v22, v51, v47 offset0:64 offset1:80
	ds_write2_b32 v22, v52, v48 offset0:128 offset1:144
	ds_write2_b32 v22, v53, v49 offset0:192 offset1:208
	ds_write2_b32 v22, v42, v38 offset0:32 offset1:48
	ds_write2_b32 v22, v43, v39 offset0:96 offset1:112
	ds_write2_b32 v22, v44, v40 offset0:160 offset1:176
	ds_write2_b32 v22, v45, v41 offset0:224 offset1:240
	v_add_u32_e32 v22, 0x3000, v119
	ds_write2_b32 v22, v34, v18 offset1:16
	ds_write2_b32 v22, v35, v19 offset0:64 offset1:80
	ds_write2_b32 v22, v36, v20 offset0:128 offset1:144
	ds_write2_b32 v22, v37, v21 offset0:192 offset1:208
	ds_write2_b32 v22, v10, v2 offset0:32 offset1:48
	ds_write2_b32 v22, v11, v3 offset0:96 offset1:112
	ds_write2_b32 v22, v12, v4 offset0:160 offset1:176
	ds_write2_b32 v22, v13, v5 offset0:224 offset1:240
	v_add_u32_e32 v2, 0x4000, v119
	ds_write2_b32 v2, v26, v14 offset1:16
	ds_write2_b32 v2, v27, v15 offset0:64 offset1:80
	ds_write2_b32 v2, v28, v16 offset0:128 offset1:144
	ds_write2_b32 v2, v29, v17 offset0:192 offset1:208
	ds_write2_b32 v2, v6, v30 offset0:32 offset1:48
	ds_write2_b32 v2, v7, v31 offset0:96 offset1:112
	ds_write2_b32 v2, v8, v32 offset0:160 offset1:176
	ds_write2_b32 v2, v9, v33 offset0:224 offset1:240
	s_waitcnt lgkmcnt(0)
	s_barrier
	ds_read_b32 v2, v120 offset:4096
	ds_read_b32 v3, v120 offset:20480
	ds_read_b32 v4, v120 offset:36864
	v_add_u32_e32 v5, 0x11000, v120
	ds_read_b32 v5, v5
	ds_read_b32 v6, v254
	ds_read_b32 v7, v121
	ds_read_b32 v8, v124
	ds_read_b32 v9, v120 offset:53248
	s_waitcnt lgkmcnt(7)
	v_add_f32_e32 v2, 0, v2
	s_waitcnt lgkmcnt(6)
	v_add_f32_e32 v2, v2, v3
	s_waitcnt lgkmcnt(5)
	v_add_f32_e32 v2, v2, v4
	s_mov_b32 s0, 0
	s_waitcnt lgkmcnt(0)
	v_add_f32_e32 v2, v2, v9
	v_add_f32_e32 v2, v2, v5
	v_add_f32_e32 v2, v2, v6
	v_add_f32_e32 v2, v2, v7
	v_add_f32_e32 v2, v2, v8
	ds_write_b32 v114, v2
	ds_read_b32 v2, v120 offset:4352
	ds_read_b32 v3, v120 offset:20736
	ds_read_b32 v4, v120 offset:37120
	ds_read_b32 v5, v125
	ds_read_b32 v6, v126
	ds_read_b32 v7, v127
	ds_read_b32 v8, v128
	ds_read_b32 v9, v120 offset:53504
	s_waitcnt lgkmcnt(7)
	v_add_f32_e32 v2, 0, v2
	s_waitcnt lgkmcnt(6)
	v_add_f32_e32 v2, v2, v3
	s_waitcnt lgkmcnt(5)
	v_add_f32_e32 v2, v2, v4
	s_waitcnt lgkmcnt(0)
	v_add_f32_e32 v2, v2, v9
	v_add_f32_e32 v2, v2, v5
	v_add_f32_e32 v2, v2, v6
	v_add_f32_e32 v2, v2, v7
	v_add_f32_e32 v2, v2, v8
	ds_write_b32 v114, v2 offset:256
	ds_read_b32 v2, v120 offset:4608
	ds_read_b32 v3, v120 offset:20992
	ds_read_b32 v4, v120 offset:37376
	ds_read_b32 v5, v129
	ds_read_b32 v6, v130
	ds_read_b32 v7, v131
	ds_read_b32 v8, v132
	ds_read_b32 v9, v120 offset:53760
	s_waitcnt lgkmcnt(7)
	v_add_f32_e32 v2, 0, v2
	s_waitcnt lgkmcnt(6)
	v_add_f32_e32 v2, v2, v3
	s_waitcnt lgkmcnt(5)
	v_add_f32_e32 v2, v2, v4
	s_waitcnt lgkmcnt(0)
	v_add_f32_e32 v2, v2, v9
	v_add_f32_e32 v2, v2, v5
	v_add_f32_e32 v2, v2, v6
	v_add_f32_e32 v2, v2, v7
	v_add_f32_e32 v2, v2, v8
	ds_write_b32 v114, v2 offset:512
	ds_read_b32 v2, v120 offset:4864
	ds_read_b32 v3, v120 offset:21248
	ds_read_b32 v4, v120 offset:37632
	ds_read_b32 v5, v133
	ds_read_b32 v6, v134
	ds_read_b32 v7, v135
	ds_read_b32 v8, v136
	ds_read_b32 v9, v120 offset:54016
	s_waitcnt lgkmcnt(7)
	v_add_f32_e32 v2, 0, v2
	s_waitcnt lgkmcnt(6)
	v_add_f32_e32 v2, v2, v3
	s_waitcnt lgkmcnt(5)
	v_add_f32_e32 v2, v2, v4
	s_waitcnt lgkmcnt(0)
	v_add_f32_e32 v2, v2, v9
	v_add_f32_e32 v2, v2, v5
	v_add_f32_e32 v2, v2, v6
	v_add_f32_e32 v2, v2, v7
	v_add_f32_e32 v2, v2, v8
	ds_write_b32 v114, v2 offset:768
	ds_read_b32 v2, v120 offset:5120
	ds_read_b32 v3, v120 offset:21504
	ds_read_b32 v4, v120 offset:37888
	ds_read_b32 v5, v137
	ds_read_b32 v6, v138
	ds_read_b32 v7, v139
	ds_read_b32 v8, v140
	ds_read_b32 v9, v120 offset:54272
	s_waitcnt lgkmcnt(7)
	v_add_f32_e32 v2, 0, v2
	s_waitcnt lgkmcnt(6)
	v_add_f32_e32 v2, v2, v3
	s_waitcnt lgkmcnt(5)
	v_add_f32_e32 v2, v2, v4
	s_waitcnt lgkmcnt(0)
	v_add_f32_e32 v2, v2, v9
	v_add_f32_e32 v2, v2, v5
	v_add_f32_e32 v2, v2, v6
	v_add_f32_e32 v2, v2, v7
	v_add_f32_e32 v2, v2, v8
	ds_write_b32 v114, v2 offset:1024
	ds_read_b32 v2, v120 offset:5376
	ds_read_b32 v3, v120 offset:21760
	ds_read_b32 v4, v120 offset:38144
	ds_read_b32 v5, v141
	ds_read_b32 v6, v142
	ds_read_b32 v7, v143
	ds_read_b32 v8, v144
	ds_read_b32 v9, v120 offset:54528
	s_waitcnt lgkmcnt(7)
	v_add_f32_e32 v2, 0, v2
	s_waitcnt lgkmcnt(6)
	v_add_f32_e32 v2, v2, v3
	s_waitcnt lgkmcnt(5)
	v_add_f32_e32 v2, v2, v4
	s_waitcnt lgkmcnt(0)
	v_add_f32_e32 v2, v2, v9
	v_add_f32_e32 v2, v2, v5
	v_add_f32_e32 v2, v2, v6
	v_add_f32_e32 v2, v2, v7
	v_add_f32_e32 v2, v2, v8
	ds_write_b32 v114, v2 offset:1280
	ds_read_b32 v2, v120 offset:5632
	ds_read_b32 v3, v120 offset:22016
	ds_read_b32 v4, v120 offset:38400
	ds_read_b32 v5, v145
	ds_read_b32 v6, v146
	ds_read_b32 v7, v147
	ds_read_b32 v8, v148
	ds_read_b32 v9, v120 offset:54784
	s_waitcnt lgkmcnt(7)
	v_add_f32_e32 v2, 0, v2
	s_waitcnt lgkmcnt(6)
	v_add_f32_e32 v2, v2, v3
	s_waitcnt lgkmcnt(5)
	v_add_f32_e32 v2, v2, v4
	s_waitcnt lgkmcnt(0)
	v_add_f32_e32 v2, v2, v9
	v_add_f32_e32 v2, v2, v5
	v_add_f32_e32 v2, v2, v6
	v_add_f32_e32 v2, v2, v7
	v_add_f32_e32 v2, v2, v8
	ds_write_b32 v114, v2 offset:1536
	ds_read_b32 v2, v120 offset:5888
	ds_read_b32 v3, v120 offset:22272
	ds_read_b32 v4, v120 offset:38656
	ds_read_b32 v5, v149
	ds_read_b32 v6, v150
	ds_read_b32 v7, v151
	ds_read_b32 v8, v152
	ds_read_b32 v9, v120 offset:55040
	s_waitcnt lgkmcnt(7)
	v_add_f32_e32 v2, 0, v2
	s_waitcnt lgkmcnt(6)
	v_add_f32_e32 v2, v2, v3
	s_waitcnt lgkmcnt(5)
	v_add_f32_e32 v2, v2, v4
	s_waitcnt lgkmcnt(0)
	v_add_f32_e32 v2, v2, v9
	v_add_f32_e32 v2, v2, v5
	v_add_f32_e32 v2, v2, v6
	v_add_f32_e32 v2, v2, v7
	v_add_f32_e32 v2, v2, v8
	ds_write_b32 v114, v2 offset:1792
	s_waitcnt lgkmcnt(0)
	v_mov_b32_e32 v6, v66
	s_branch .LBB0_1031
